# combo17 + gate-up K-loop: gathered-row table ds_read_b32 issued right after the first fragment read, counted lgkmcnt(15) instead of draining all 16 fragment reads before the LDS-DMA issue (phases 1 an
# baseline (speedup 1.0000x reference)
.LBB0_1034:
	v_readfirstlane_b32 s19, v4
	s_xor_b32 s27, s75, s19
	s_lshl_b32 s19, s75, 12
	s_add_i32 s74, s19, 0
	s_add_i32 s74, s74, 0x21000
	s_add_u32 s19, s24, 0x100
	s_addc_u32 s76, s25, 0
	s_mov_b32 s77, -2
	s_mov_b64 s[24:25], s[14:15]
	ds_read_b128 v[136:139], v150
	s_waitcnt vmcnt(0)
	v_mbcnt_lo_u32_b32 v40, -1, 0
	v_mbcnt_hi_u32_b32 v40, -1, v40
	s_mov_b32 s78, s61
	v_lshlrev_b32_e32 v40, 3, v40
	s_add_i32 m0, s35, 0xc000
	v_lshl_or_b32 v40, s78, 9, v40
	v_add_u32_e32 v40, s74, v40
	ds_read_b32 v40, v40 offset:4
	ds_read_b128 v[156:159], v150 offset:2048
	ds_read_b128 v[140:143], v151
	ds_read_b128 v[160:163], v151 offset:2048
	ds_read_b128 v[164:167], v150 offset:16384
	ds_read_b128 v[172:175], v150 offset:18432
	ds_read_b128 v[168:171], v151 offset:16384
	ds_read_b128 v[176:179], v151 offset:18432
	s_add_u32 s28, s24, 0x80
	s_addc_u32 s29, s25, 0
	s_cmp_eq_u32 s77, 4
	s_cselect_b32 s29, s11, s29
	s_cselect_b32 s28, s10, s28
	s_cselect_b32 s80, s27, s75
	s_cselect_b32 s37, s23, s76
	s_cselect_b32 s36, s22, s19
	ds_read_b128 v[194:197], v148
	ds_read_b128 v[228:231], v148 offset:2048
	ds_read_b128 v[198:201], v149
	ds_read_b128 v[232:235], v149 offset:2048
	ds_read_b128 v[236:239], v148 offset:4096
	ds_read_b128 v[244:247], v148 offset:6144
	ds_read_b128 v[240:243], v149 offset:4096
	ds_read_b128 v[248:251], v149 offset:6144
	s_waitcnt lgkmcnt(15)
	v_lshlrev_b32_e32 v41, 10, v40
	v_and_or_b32 v41, v41, s69, v154
	v_bfe_u32 v40, v40, 16, 16
	v_lshl_or_b32 v40, v40, 10, v154
	global_load_lds_dwordx4 v41, s[24:25]
	s_add_i32 m0, s35, 0xe000
	s_nop 0
	global_load_lds_dwordx4 v40, s[24:25]
	s_waitcnt vmcnt(8)
	s_waitcnt lgkmcnt(0)
	s_barrier
	s_setprio 1
	v_mfma_f32_16x16x128_f8f6f4 v[132:135], v[136:143], v[194:201], 0
	v_mfma_f32_16x16x128_f8f6f4 v[124:127], v[156:163], v[194:201], 0
	v_mfma_f32_16x16x128_f8f6f4 v[116:119], v[136:143], v[228:235], 0
	v_mfma_f32_16x16x128_f8f6f4 v[108:111], v[156:163], v[228:235], 0
	v_mfma_f32_16x16x128_f8f6f4 v[144:147], v[136:143], v[236:243], 0
	v_mfma_f32_16x16x128_f8f6f4 v[180:183], v[156:163], v[236:243], 0
	v_mfma_f32_16x16x128_f8f6f4 v[186:189], v[136:143], v[244:251], 0
	v_mfma_f32_16x16x128_f8f6f4 v[190:193], v[156:163], v[244:251], 0
	s_setprio 0
	s_setprio 1
	v_mfma_f32_16x16x128_f8f6f4 v[128:131], v[164:171], v[194:201], 0
	v_mfma_f32_16x16x128_f8f6f4 v[120:123], v[172:179], v[194:201], 0
	v_mfma_f32_16x16x128_f8f6f4 v[112:115], v[164:171], v[228:235], 0
	v_mfma_f32_16x16x128_f8f6f4 v[104:107], v[172:179], v[228:235], 0
	v_mfma_f32_16x16x128_f8f6f4 v[202:205], v[164:171], v[236:243], 0
	v_mfma_f32_16x16x128_f8f6f4 v[206:209], v[172:179], v[236:243], 0
	v_mfma_f32_16x16x128_f8f6f4 v[210:213], v[164:171], v[244:251], 0
	v_mfma_f32_16x16x128_f8f6f4 v[214:217], v[172:179], v[244:251], 0
	s_setprio 0
	s_barrier
	v_mov_b32_e32 v40, v152
	s_mov_b32 m0, s44
	s_nop 2
	ds_read_b128 v[72:75], v148 offset:16384
	ds_read_b128 v[80:83], v148 offset:18432
	ds_read_b128 v[76:79], v149 offset:16384
	ds_read_b128 v[84:87], v149 offset:18432
	ds_read_b128 v[88:91], v148 offset:20480
	ds_read_b128 v[96:99], v148 offset:22528
	ds_read_b128 v[92:95], v149 offset:20480
	ds_read_b128 v[100:103], v149 offset:22528
	s_add_u32 s78, s36, 0x20000
	global_load_lds_dwordx4 v40, s[36:37]
	v_mov_b32_e32 v40, v153
	s_mov_b32 m0, s49
	s_addc_u32 s79, s37, 0
	global_load_lds_dwordx4 v40, s[36:37]
	v_mov_b32_e32 v40, v152
	s_mov_b32 m0, s50
	s_nop 0
	global_load_lds_dwordx4 v40, s[78:79]
	v_mov_b32_e32 v40, v153
	s_mov_b32 m0, s51
	s_nop 0
	global_load_lds_dwordx4 v40, s[78:79]
	v_mbcnt_lo_u32_b32 v40, -1, 0
	v_mbcnt_hi_u32_b32 v40, -1, v40
	s_mov_b32 s78, s61
	v_lshlrev_b32_e32 v40, 3, v40
	v_lshl_or_b32 v40, s78, 9, v40
	s_lshl_b32 s78, s80, 12
	s_add_i32 s78, s78, 0
	s_add_i32 s78, s78, 0x21000
	v_add_u32_e32 v40, s78, v40
	ds_read_b32 v40, v40
	s_mov_b32 m0, s35
	s_waitcnt lgkmcnt(0)
	v_lshlrev_b32_e32 v41, 10, v40
	v_and_or_b32 v41, v41, s69, v154
	v_bfe_u32 v40, v40, 16, 16
	v_lshl_or_b32 v40, v40, 10, v154
	global_load_lds_dwordx4 v41, s[28:29]
	s_mov_b32 m0, s54
	s_nop 0
	global_load_lds_dwordx4 v40, s[28:29]
	s_waitcnt vmcnt(8)
	s_waitcnt lgkmcnt(0)
	s_barrier
	s_setprio 1
	v_mfma_f32_16x16x128_f8f6f4 v[48:51], v[136:143], v[80:87], 0
	v_mfma_f32_16x16x128_f8f6f4 v[36:39], v[156:163], v[80:87], 0
	v_mfma_f32_16x16x128_f8f6f4 v[28:31], v[136:143], v[88:95], 0
	v_mfma_f32_16x16x128_f8f6f4 v[20:23], v[156:163], v[88:95], 0
	v_mfma_f32_16x16x128_f8f6f4 v[12:15], v[136:143], v[96:103], 0
	v_mfma_f32_16x16x128_f8f6f4 v[4:7], v[156:163], v[96:103], 0
	v_mfma_f32_16x16x128_f8f6f4 v[40:43], v[136:143], v[72:79], 0
	v_mfma_f32_16x16x128_f8f6f4 v[52:55], v[156:163], v[72:79], 0
	s_setprio 0
	s_setprio 1
	v_mfma_f32_16x16x128_f8f6f4 v[64:67], v[164:171], v[72:79], 0
	v_mfma_f32_16x16x128_f8f6f4 v[56:59], v[172:179], v[72:79], 0
	v_mfma_f32_16x16x128_f8f6f4 v[44:47], v[164:171], v[80:87], 0
	v_mfma_f32_16x16x128_f8f6f4 v[32:35], v[172:179], v[80:87], 0
	v_mfma_f32_16x16x128_f8f6f4 v[24:27], v[164:171], v[88:95], 0
	v_mfma_f32_16x16x128_f8f6f4 v[16:19], v[172:179], v[88:95], 0
	v_mfma_f32_16x16x128_f8f6f4 v[8:11], v[164:171], v[96:103], 0
	v_mfma_f32_16x16x128_f8f6f4 v[0:3], v[172:179], v[96:103], 0
	s_setprio 0
	s_barrier
	ds_read_b128 v[136:139], v150 offset:32768
	v_mbcnt_lo_u32_b32 v60, -1, 0
	v_mbcnt_hi_u32_b32 v60, -1, v60
	s_mov_b32 s79, s61
	v_lshlrev_b32_e32 v60, 3, v60
	s_mov_b32 m0, s55
	v_lshl_or_b32 v60, s79, 9, v60
	v_add_u32_e32 v60, s78, v60
	ds_read_b32 v60, v60 offset:4
	ds_read_b128 v[156:159], v150 offset:34816
	ds_read_b128 v[140:143], v151 offset:32768
	ds_read_b128 v[160:163], v151 offset:34816
	ds_read_b128 v[164:167], v150 offset:49152
	ds_read_b128 v[172:175], v150 offset:51200
	ds_read_b128 v[168:171], v151 offset:49152
	ds_read_b128 v[176:179], v151 offset:51200
	ds_read_b128 v[68:71], v148 offset:32768
	ds_read_b128 v[194:197], v148 offset:34816
	ds_read_b128 v[72:75], v149 offset:32768
	ds_read_b128 v[198:201], v149 offset:34816
	ds_read_b128 v[228:231], v148 offset:36864
	ds_read_b128 v[236:239], v148 offset:38912
	ds_read_b128 v[232:235], v149 offset:36864
	ds_read_b128 v[240:243], v149 offset:38912
	s_waitcnt lgkmcnt(15)
	v_lshlrev_b32_e32 v61, 10, v60
	v_and_or_b32 v61, v61, s69, v154
	v_bfe_u32 v60, v60, 16, 16
	v_lshl_or_b32 v60, v60, 10, v154
	global_load_lds_dwordx4 v61, s[28:29]
	s_mov_b32 m0, s56
	s_nop 0
	global_load_lds_dwordx4 v60, s[28:29]
	s_waitcnt vmcnt(8)
	s_waitcnt lgkmcnt(0)
	s_barrier
	s_setprio 1
	v_mfma_f32_16x16x128_f8f6f4 v[132:135], v[136:143], v[68:75], v[132:135]
	v_mfma_f32_16x16x128_f8f6f4 v[124:127], v[156:163], v[68:75], v[124:127]
	v_mfma_f32_16x16x128_f8f6f4 v[116:119], v[136:143], v[194:201], v[116:119]
	v_mfma_f32_16x16x128_f8f6f4 v[108:111], v[156:163], v[194:201], v[108:111]
	v_mfma_f32_16x16x128_f8f6f4 v[100:103], v[136:143], v[228:235], v[144:147]
	v_mfma_f32_16x16x128_f8f6f4 v[92:95], v[156:163], v[228:235], v[180:183]
	v_mfma_f32_16x16x128_f8f6f4 v[84:87], v[136:143], v[236:243], v[186:189]
	v_mfma_f32_16x16x128_f8f6f4 v[76:79], v[156:163], v[236:243], v[190:193]
	s_setprio 0
	s_setprio 1
	v_mfma_f32_16x16x128_f8f6f4 v[128:131], v[164:171], v[68:75], v[128:131]
	v_mfma_f32_16x16x128_f8f6f4 v[120:123], v[172:179], v[68:75], v[120:123]
	v_mfma_f32_16x16x128_f8f6f4 v[112:115], v[164:171], v[194:201], v[112:115]
	v_mfma_f32_16x16x128_f8f6f4 v[104:107], v[172:179], v[194:201], v[104:107]
	v_mfma_f32_16x16x128_f8f6f4 v[96:99], v[164:171], v[228:235], v[202:205]
	v_mfma_f32_16x16x128_f8f6f4 v[88:91], v[172:179], v[228:235], v[206:209]
	v_mfma_f32_16x16x128_f8f6f4 v[80:83], v[164:171], v[236:243], v[210:213]
	v_mfma_f32_16x16x128_f8f6f4 v[72:75], v[172:179], v[236:243], v[214:217]
	s_setprio 0
	s_barrier
	v_mov_b32_e32 v184, v152
	ds_read_b128 v[194:197], v148 offset:49152
	ds_read_b128 v[228:231], v148 offset:51200
	ds_read_b128 v[198:201], v149 offset:49152
	ds_read_b128 v[232:235], v149 offset:51200
	ds_read_b128 v[236:239], v148 offset:53248
	ds_read_b128 v[244:247], v148 offset:55296
	ds_read_b128 v[240:243], v149 offset:53248
	ds_read_b128 v[248:251], v149 offset:55296
	s_mov_b32 m0, s57
	v_lshl_add_u64 v[60:61], s[36:37], 0, v[184:185]
	v_lshl_add_u64 v[60:61], v[60:61], 0, s[46:47]
	v_mov_b32_e32 v184, v153
	global_load_lds_dwordx4 v[60:61], off
	s_mov_b32 m0, s59
	v_lshl_add_u64 v[60:61], s[36:37], 0, v[184:185]
	v_lshl_add_u64 v[60:61], v[60:61], 0, s[46:47]
	global_load_lds_dwordx4 v[60:61], off
	s_add_u32 s36, s36, 0x20080
	v_mov_b32_e32 v60, v152
	s_addc_u32 s37, s37, 0
	s_mov_b32 m0, s66
	s_nop 0
	global_load_lds_dwordx4 v60, s[36:37]
	v_mov_b32_e32 v60, v153
	s_mov_b32 m0, s67
	s_nop 0
	global_load_lds_dwordx4 v60, s[36:37]
	v_mbcnt_lo_u32_b32 v60, -1, 0
	v_mbcnt_hi_u32_b32 v60, -1, v60
	s_mov_b32 s36, s61
	v_lshlrev_b32_e32 v60, 3, v60
	s_mov_b32 m0, s64
	v_lshl_or_b32 v60, s36, 9, v60
	v_add_u32_e32 v60, s78, v60
	ds_read_b32 v62, v60
	s_waitcnt lgkmcnt(0)
	v_lshlrev_b32_e32 v60, 10, v62
	v_and_or_b32 v184, v60, s69, v154
	s_nop 0
	v_lshl_add_u64 v[60:61], s[28:29], 0, v[184:185]
	v_lshl_add_u64 v[60:61], v[60:61], 0, s[46:47]
	global_load_lds_dwordx4 v[60:61], off
	v_bfe_u32 v60, v62, 16, 16
	v_lshl_or_b32 v184, v60, 10, v154
	s_mov_b32 m0, s65
	v_lshl_add_u64 v[60:61], s[28:29], 0, v[184:185]
	v_lshl_add_u64 v[60:61], v[60:61], 0, s[46:47]
	global_load_lds_dwordx4 v[60:61], off
	s_waitcnt vmcnt(8)
	s_waitcnt lgkmcnt(0)
	s_barrier
	s_setprio 1
	v_mfma_f32_16x16x128_f8f6f4 v[68:71], v[136:143], v[194:201], v[40:43]
	v_mfma_f32_16x16x128_f8f6f4 v[60:63], v[156:163], v[194:201], v[52:55]
	v_mfma_f32_16x16x128_f8f6f4 v[48:51], v[136:143], v[228:235], v[48:51]
	v_mfma_f32_16x16x128_f8f6f4 v[36:39], v[156:163], v[228:235], v[36:39]
	v_mfma_f32_16x16x128_f8f6f4 v[28:31], v[136:143], v[236:243], v[28:31]
	v_mfma_f32_16x16x128_f8f6f4 v[20:23], v[156:163], v[236:243], v[20:23]
	v_mfma_f32_16x16x128_f8f6f4 v[12:15], v[136:143], v[244:251], v[12:15]
	v_mfma_f32_16x16x128_f8f6f4 v[4:7], v[156:163], v[244:251], v[4:7]
	s_setprio 0
	s_setprio 1
	v_mfma_f32_16x16x128_f8f6f4 v[64:67], v[164:171], v[194:201], v[64:67]
	v_mfma_f32_16x16x128_f8f6f4 v[56:59], v[172:179], v[194:201], v[56:59]
	v_mfma_f32_16x16x128_f8f6f4 v[44:47], v[164:171], v[228:235], v[44:47]
	v_mfma_f32_16x16x128_f8f6f4 v[32:35], v[172:179], v[228:235], v[32:35]
	v_mfma_f32_16x16x128_f8f6f4 v[24:27], v[164:171], v[236:243], v[24:27]
	v_mfma_f32_16x16x128_f8f6f4 v[16:19], v[172:179], v[236:243], v[16:19]
	v_mfma_f32_16x16x128_f8f6f4 v[8:11], v[164:171], v[244:251], v[8:11]
	v_mfma_f32_16x16x128_f8f6f4 v[0:3], v[172:179], v[244:251], v[0:3]
	s_setprio 0
	s_barrier
	s_add_i32 s77, s77, 2
	s_add_u32 s24, s24, 0x100
	s_addc_u32 s25, s25, 0
	s_add_u32 s19, s19, 0x100
	s_addc_u32 s76, s76, 0
.LBB0_1035:
	ds_read_b128 v[136:139], v150
	v_mbcnt_lo_u32_b32 v40, -1, 0
	v_mbcnt_hi_u32_b32 v40, -1, v40
	s_mov_b32 s78, s61
	v_lshlrev_b32_e32 v40, 3, v40
	s_add_i32 m0, s35, 0xc000
	v_lshl_or_b32 v40, s78, 9, v40
	v_add_u32_e32 v40, s74, v40
	ds_read_b32 v40, v40 offset:4
	ds_read_b128 v[156:159], v150 offset:2048
	ds_read_b128 v[140:143], v151
	ds_read_b128 v[160:163], v151 offset:2048
	ds_read_b128 v[164:167], v150 offset:16384
	ds_read_b128 v[172:175], v150 offset:18432
	ds_read_b128 v[168:171], v151 offset:16384
	ds_read_b128 v[176:179], v151 offset:18432
	s_add_u32 s28, s24, 0x80
	s_addc_u32 s29, s25, 0
	s_cmp_eq_u32 s77, 4
	s_cselect_b32 s29, s11, s29
	s_cselect_b32 s28, s10, s28
	s_cselect_b32 s80, s27, s75
	s_cselect_b32 s37, s23, s76
	s_cselect_b32 s36, s22, s19
	ds_read_b128 v[194:197], v148
	ds_read_b128 v[228:231], v148 offset:2048
	ds_read_b128 v[198:201], v149
	ds_read_b128 v[232:235], v149 offset:2048
	ds_read_b128 v[236:239], v148 offset:4096
	ds_read_b128 v[244:247], v148 offset:6144
	ds_read_b128 v[240:243], v149 offset:4096
	ds_read_b128 v[248:251], v149 offset:6144
	s_waitcnt lgkmcnt(15)
	v_lshlrev_b32_e32 v41, 10, v40
	v_and_or_b32 v41, v41, s69, v154
	v_bfe_u32 v40, v40, 16, 16
	v_lshl_or_b32 v40, v40, 10, v154
	global_load_lds_dwordx4 v41, s[24:25]
	s_add_i32 m0, s35, 0xe000
	s_nop 0
	global_load_lds_dwordx4 v40, s[24:25]
	s_waitcnt vmcnt(8)
	s_waitcnt lgkmcnt(0)
	s_barrier
	s_setprio 1
	v_mfma_f32_16x16x128_f8f6f4 v[132:135], v[136:143], v[194:201], v[132:135]
	v_mfma_f32_16x16x128_f8f6f4 v[124:127], v[156:163], v[194:201], v[124:127]
	v_mfma_f32_16x16x128_f8f6f4 v[116:119], v[136:143], v[228:235], v[116:119]
	v_mfma_f32_16x16x128_f8f6f4 v[108:111], v[156:163], v[228:235], v[108:111]
	v_mfma_f32_16x16x128_f8f6f4 v[144:147], v[136:143], v[236:243], v[100:103]
	v_mfma_f32_16x16x128_f8f6f4 v[180:183], v[156:163], v[236:243], v[92:95]
	v_mfma_f32_16x16x128_f8f6f4 v[186:189], v[136:143], v[244:251], v[84:87]
	v_mfma_f32_16x16x128_f8f6f4 v[190:193], v[156:163], v[244:251], v[76:79]
	s_setprio 0
	s_setprio 1
	v_mfma_f32_16x16x128_f8f6f4 v[128:131], v[164:171], v[194:201], v[128:131]
	v_mfma_f32_16x16x128_f8f6f4 v[120:123], v[172:179], v[194:201], v[120:123]
	v_mfma_f32_16x16x128_f8f6f4 v[112:115], v[164:171], v[228:235], v[112:115]
	v_mfma_f32_16x16x128_f8f6f4 v[104:107], v[172:179], v[228:235], v[104:107]
	v_mfma_f32_16x16x128_f8f6f4 v[202:205], v[164:171], v[236:243], v[96:99]
	v_mfma_f32_16x16x128_f8f6f4 v[206:209], v[172:179], v[236:243], v[88:91]
	v_mfma_f32_16x16x128_f8f6f4 v[210:213], v[164:171], v[244:251], v[80:83]
	v_mfma_f32_16x16x128_f8f6f4 v[214:217], v[172:179], v[244:251], v[72:75]
	s_setprio 0
	s_barrier
	v_mov_b32_e32 v40, v152
	s_mov_b32 m0, s44
	s_nop 2
	ds_read_b128 v[72:75], v148 offset:16384
	ds_read_b128 v[80:83], v148 offset:18432
	ds_read_b128 v[76:79], v149 offset:16384
	ds_read_b128 v[84:87], v149 offset:18432
	ds_read_b128 v[88:91], v148 offset:20480
	ds_read_b128 v[96:99], v148 offset:22528
	ds_read_b128 v[92:95], v149 offset:20480
	ds_read_b128 v[100:103], v149 offset:22528
	s_add_u32 s78, s36, 0x20000
	global_load_lds_dwordx4 v40, s[36:37]
	v_mov_b32_e32 v40, v153
	s_mov_b32 m0, s49
	s_addc_u32 s79, s37, 0
	global_load_lds_dwordx4 v40, s[36:37]
	v_mov_b32_e32 v40, v152
	s_mov_b32 m0, s50
	s_nop 0
	global_load_lds_dwordx4 v40, s[78:79]
	v_mov_b32_e32 v40, v153
	s_mov_b32 m0, s51
	s_nop 0
	global_load_lds_dwordx4 v40, s[78:79]
	v_mbcnt_lo_u32_b32 v40, -1, 0
	v_mbcnt_hi_u32_b32 v40, -1, v40
	s_mov_b32 s78, s61
	v_lshlrev_b32_e32 v40, 3, v40
	v_lshl_or_b32 v40, s78, 9, v40
	s_lshl_b32 s78, s80, 12
	s_add_i32 s78, s78, 0
	s_add_i32 s78, s78, 0x21000
	v_add_u32_e32 v40, s78, v40
	ds_read_b32 v40, v40
	s_mov_b32 m0, s35
	s_waitcnt lgkmcnt(0)
	v_lshlrev_b32_e32 v41, 10, v40
	v_and_or_b32 v41, v41, s69, v154
	v_bfe_u32 v40, v40, 16, 16
	v_lshl_or_b32 v40, v40, 10, v154
	global_load_lds_dwordx4 v41, s[28:29]
	s_mov_b32 m0, s54
	s_nop 0
	global_load_lds_dwordx4 v40, s[28:29]
	s_waitcnt vmcnt(8)
	s_waitcnt lgkmcnt(0)
	s_barrier
	s_setprio 1
	v_mfma_f32_16x16x128_f8f6f4 v[48:51], v[136:143], v[80:87], v[48:51]
	v_mfma_f32_16x16x128_f8f6f4 v[36:39], v[156:163], v[80:87], v[36:39]
	v_mfma_f32_16x16x128_f8f6f4 v[28:31], v[136:143], v[88:95], v[28:31]
	v_mfma_f32_16x16x128_f8f6f4 v[20:23], v[156:163], v[88:95], v[20:23]
	v_mfma_f32_16x16x128_f8f6f4 v[12:15], v[136:143], v[96:103], v[12:15]
	v_mfma_f32_16x16x128_f8f6f4 v[4:7], v[156:163], v[96:103], v[4:7]
	v_mfma_f32_16x16x128_f8f6f4 v[40:43], v[136:143], v[72:79], v[68:71]
	v_mfma_f32_16x16x128_f8f6f4 v[52:55], v[156:163], v[72:79], v[60:63]
	s_setprio 0
	s_setprio 1
	v_mfma_f32_16x16x128_f8f6f4 v[64:67], v[164:171], v[72:79], v[64:67]
	v_mfma_f32_16x16x128_f8f6f4 v[56:59], v[172:179], v[72:79], v[56:59]
	v_mfma_f32_16x16x128_f8f6f4 v[44:47], v[164:171], v[80:87], v[44:47]
	v_mfma_f32_16x16x128_f8f6f4 v[32:35], v[172:179], v[80:87], v[32:35]
	v_mfma_f32_16x16x128_f8f6f4 v[24:27], v[164:171], v[88:95], v[24:27]
	v_mfma_f32_16x16x128_f8f6f4 v[16:19], v[172:179], v[88:95], v[16:19]
	v_mfma_f32_16x16x128_f8f6f4 v[8:11], v[164:171], v[96:103], v[8:11]
	v_mfma_f32_16x16x128_f8f6f4 v[0:3], v[172:179], v[96:103], v[0:3]
	s_setprio 0
	s_barrier
	ds_read_b128 v[136:139], v150 offset:32768
	v_mbcnt_lo_u32_b32 v60, -1, 0
	v_mbcnt_hi_u32_b32 v60, -1, v60
	s_mov_b32 s79, s61
	v_lshlrev_b32_e32 v60, 3, v60
	s_mov_b32 m0, s55
	v_lshl_or_b32 v60, s79, 9, v60
	v_add_u32_e32 v60, s78, v60
	ds_read_b32 v60, v60 offset:4
	ds_read_b128 v[156:159], v150 offset:34816
	ds_read_b128 v[140:143], v151 offset:32768
	ds_read_b128 v[160:163], v151 offset:34816
	ds_read_b128 v[164:167], v150 offset:49152
	ds_read_b128 v[172:175], v150 offset:51200
	ds_read_b128 v[168:171], v151 offset:49152
	ds_read_b128 v[176:179], v151 offset:51200
	ds_read_b128 v[68:71], v148 offset:32768
	ds_read_b128 v[194:197], v148 offset:34816
	ds_read_b128 v[72:75], v149 offset:32768
	ds_read_b128 v[198:201], v149 offset:34816
	ds_read_b128 v[228:231], v148 offset:36864
	ds_read_b128 v[236:239], v148 offset:38912
	ds_read_b128 v[232:235], v149 offset:36864
	ds_read_b128 v[240:243], v149 offset:38912
	s_waitcnt lgkmcnt(15)
	v_lshlrev_b32_e32 v61, 10, v60
	v_and_or_b32 v61, v61, s69, v154
	v_bfe_u32 v60, v60, 16, 16
	v_lshl_or_b32 v60, v60, 10, v154
	global_load_lds_dwordx4 v61, s[28:29]
	s_mov_b32 m0, s56
	s_nop 0
	global_load_lds_dwordx4 v60, s[28:29]
	s_waitcnt vmcnt(8)
	s_waitcnt lgkmcnt(0)
	s_barrier
	s_setprio 1
	v_mfma_f32_16x16x128_f8f6f4 v[132:135], v[136:143], v[68:75], v[132:135]
	v_mfma_f32_16x16x128_f8f6f4 v[124:127], v[156:163], v[68:75], v[124:127]
	v_mfma_f32_16x16x128_f8f6f4 v[116:119], v[136:143], v[194:201], v[116:119]
	v_mfma_f32_16x16x128_f8f6f4 v[108:111], v[156:163], v[194:201], v[108:111]
	v_mfma_f32_16x16x128_f8f6f4 v[100:103], v[136:143], v[228:235], v[144:147]
	v_mfma_f32_16x16x128_f8f6f4 v[92:95], v[156:163], v[228:235], v[180:183]
	v_mfma_f32_16x16x128_f8f6f4 v[84:87], v[136:143], v[236:243], v[186:189]
	v_mfma_f32_16x16x128_f8f6f4 v[76:79], v[156:163], v[236:243], v[190:193]
	s_setprio 0
	s_setprio 1
	v_mfma_f32_16x16x128_f8f6f4 v[128:131], v[164:171], v[68:75], v[128:131]
	v_mfma_f32_16x16x128_f8f6f4 v[120:123], v[172:179], v[68:75], v[120:123]
	v_mfma_f32_16x16x128_f8f6f4 v[112:115], v[164:171], v[194:201], v[112:115]
	v_mfma_f32_16x16x128_f8f6f4 v[104:107], v[172:179], v[194:201], v[104:107]
	v_mfma_f32_16x16x128_f8f6f4 v[96:99], v[164:171], v[228:235], v[202:205]
	v_mfma_f32_16x16x128_f8f6f4 v[88:91], v[172:179], v[228:235], v[206:209]
	v_mfma_f32_16x16x128_f8f6f4 v[80:83], v[164:171], v[236:243], v[210:213]
	v_mfma_f32_16x16x128_f8f6f4 v[72:75], v[172:179], v[236:243], v[214:217]
	s_setprio 0
	s_barrier
	v_mov_b32_e32 v184, v152
	ds_read_b128 v[194:197], v148 offset:49152
	ds_read_b128 v[228:231], v148 offset:51200
	ds_read_b128 v[198:201], v149 offset:49152
	ds_read_b128 v[232:235], v149 offset:51200
	ds_read_b128 v[236:239], v148 offset:53248
	ds_read_b128 v[244:247], v148 offset:55296
	ds_read_b128 v[240:243], v149 offset:53248
	ds_read_b128 v[248:251], v149 offset:55296
	s_mov_b32 m0, s57
	v_lshl_add_u64 v[60:61], s[36:37], 0, v[184:185]
	v_lshl_add_u64 v[60:61], v[60:61], 0, s[46:47]
	v_mov_b32_e32 v184, v153
	global_load_lds_dwordx4 v[60:61], off
	s_mov_b32 m0, s59
	v_lshl_add_u64 v[60:61], s[36:37], 0, v[184:185]
	v_lshl_add_u64 v[60:61], v[60:61], 0, s[46:47]
	global_load_lds_dwordx4 v[60:61], off
	s_add_u32 s36, s36, 0x20080
	v_mov_b32_e32 v60, v152
	s_addc_u32 s37, s37, 0
	s_mov_b32 m0, s66
	s_nop 0
	global_load_lds_dwordx4 v60, s[36:37]
	v_mov_b32_e32 v60, v153
	s_mov_b32 m0, s67
	s_nop 0
	global_load_lds_dwordx4 v60, s[36:37]
	v_mbcnt_lo_u32_b32 v60, -1, 0
	v_mbcnt_hi_u32_b32 v60, -1, v60
	s_mov_b32 s36, s61
	v_lshlrev_b32_e32 v60, 3, v60
	s_mov_b32 m0, s64
	v_lshl_or_b32 v60, s36, 9, v60
	v_add_u32_e32 v60, s78, v60
	ds_read_b32 v62, v60
	s_waitcnt lgkmcnt(0)
	v_lshlrev_b32_e32 v60, 10, v62
	v_and_or_b32 v184, v60, s69, v154
	s_nop 0
	v_lshl_add_u64 v[60:61], s[28:29], 0, v[184:185]
	v_lshl_add_u64 v[60:61], v[60:61], 0, s[46:47]
	global_load_lds_dwordx4 v[60:61], off
	v_bfe_u32 v60, v62, 16, 16
	v_lshl_or_b32 v184, v60, 10, v154
	s_mov_b32 m0, s65
	v_lshl_add_u64 v[60:61], s[28:29], 0, v[184:185]
	v_lshl_add_u64 v[60:61], v[60:61], 0, s[46:47]
	global_load_lds_dwordx4 v[60:61], off
	s_waitcnt vmcnt(8)
	s_waitcnt lgkmcnt(0)
	s_barrier
	s_setprio 1
	v_mfma_f32_16x16x128_f8f6f4 v[68:71], v[136:143], v[194:201], v[40:43]
	v_mfma_f32_16x16x128_f8f6f4 v[60:63], v[156:163], v[194:201], v[52:55]
	v_mfma_f32_16x16x128_f8f6f4 v[48:51], v[136:143], v[228:235], v[48:51]
	v_mfma_f32_16x16x128_f8f6f4 v[36:39], v[156:163], v[228:235], v[36:39]
	v_mfma_f32_16x16x128_f8f6f4 v[28:31], v[136:143], v[236:243], v[28:31]
	v_mfma_f32_16x16x128_f8f6f4 v[20:23], v[156:163], v[236:243], v[20:23]
	v_mfma_f32_16x16x128_f8f6f4 v[12:15], v[136:143], v[244:251], v[12:15]
	v_mfma_f32_16x16x128_f8f6f4 v[4:7], v[156:163], v[244:251], v[4:7]
	s_setprio 0
	s_setprio 1
	v_mfma_f32_16x16x128_f8f6f4 v[64:67], v[164:171], v[194:201], v[64:67]
	v_mfma_f32_16x16x128_f8f6f4 v[56:59], v[172:179], v[194:201], v[56:59]
	v_mfma_f32_16x16x128_f8f6f4 v[44:47], v[164:171], v[228:235], v[44:47]
	v_mfma_f32_16x16x128_f8f6f4 v[32:35], v[172:179], v[228:235], v[32:35]
	v_mfma_f32_16x16x128_f8f6f4 v[24:27], v[164:171], v[236:243], v[24:27]
	v_mfma_f32_16x16x128_f8f6f4 v[16:19], v[172:179], v[236:243], v[16:19]
	v_mfma_f32_16x16x128_f8f6f4 v[8:11], v[164:171], v[244:251], v[8:11]
	v_mfma_f32_16x16x128_f8f6f4 v[0:3], v[172:179], v[244:251], v[0:3]
	s_setprio 0
	s_barrier
	s_add_i32 s77, s77, 2
	s_add_u32 s24, s24, 0x100
	s_addc_u32 s25, s25, 0
	s_add_u32 s19, s19, 0x100
	s_addc_u32 s76, s76, 0
	s_cmp_gt_u32 s77, 5
	s_cbranch_scc0 .LBB0_1035
	s_and_b64 vcc, exec, s[8:9]
	s_mov_b32 s36, s26
	s_mov_b32 s28, s73
	s_mov_b64 s[8:9], 0
	s_cbranch_vccz .LBB0_1039
	s_add_i32 s8, s72, 2
	s_mul_i32 s9, s8, s31
	s_mul_hi_u32 s19, s8, s0
	s_add_i32 s19, s19, s9
	s_mul_i32 s8, s8, s0
	s_add_u32 s24, s8, s1
	s_addc_u32 s25, s19, s40
	v_mov_b64_e32 v[40:41], s[4:5]
	v_cmp_ge_i64_e32 vcc, s[24:25], v[40:41]
	s_mov_b64 s[8:9], 0
	s_mov_b32 s28, s73
	s_mov_b32 s36, s26
	s_cbranch_vccnz .LBB0_1039
	s_ashr_i32 s8, s24, 31
	s_lshr_b32 s8, s8, 29
	s_add_i32 s8, s24, s8
	s_ashr_i32 s9, s8, 3
	s_and_b32 s8, s8, -8
	s_sub_i32 s8, s24, s8
	s_lshr_b32 s19, s8, 31
	s_add_i32 s19, s33, s19
	s_mul_i32 s8, s19, s8
	s_add_i32 s8, s8, s9
	s_ashr_i32 s9, s8, 31
	s_lshr_b32 s9, s9, 26
	s_add_i32 s9, s8, s9
	s_ashr_i32 s19, s9, 6
	s_lshl_b32 s19, s19, 3
	s_sub_i32 s24, s33, s19
	s_min_i32 s24, s24, 8
	s_abs_i32 s25, s24
	v_cvt_f32_u32_e32 v40, s25
	s_sub_i32 s29, 0, s25
	s_andn2_b32 s9, s9, 63
	s_sub_i32 s8, s8, s9
	v_rcp_iflag_f32_e32 v40, v40
	s_abs_i32 s9, s8
	s_xor_b32 s28, s8, s24
	s_ashr_i32 s28, s28, 31
	v_mul_f32_e32 v40, 0x4f7ffffe, v40
	v_cvt_u32_f32_e32 v40, v40
	s_nop 0
	v_readfirstlane_b32 s36, v40
	s_mul_i32 s29, s29, s36
	s_mul_hi_u32 s29, s36, s29
	s_add_i32 s36, s36, s29
	s_mul_hi_u32 s29, s9, s36
	s_mul_i32 s36, s29, s25
	s_sub_i32 s9, s9, s36
	s_add_i32 s37, s29, 1
	s_sub_i32 s36, s9, s25
	s_cmp_ge_u32 s9, s25
	s_cselect_b32 s29, s37, s29
	s_cselect_b32 s9, s36, s9
	s_add_i32 s36, s29, 1
	s_cmp_ge_u32 s9, s25
	s_cselect_b32 s9, s36, s29
	s_xor_b32 s9, s9, s28
	s_sub_i32 s36, s9, s28
	s_mul_i32 s9, s36, s24
	s_sub_i32 s8, s8, s9
	s_add_i32 s28, s8, s19
	s_mov_b64 s[8:9], -1
